# MoE down GEMM layer 0: last partial round reassigned to the workgroups that already hold a half-unit (per-WG load max 5.0 -> 4.55 units)
# baseline (speedup 1.0000x reference)
;     __device__ bool next(int i, Unit& u) const {
;         const long L0 = (long)i * G + c; if (L0 >= nwg) return false;
;         int L = (int)L0; { const int q = nwg / NXCD, r = nwg % NXCD, xcd = L % NXCD, off = L / NXCD; L = (xcd < r ? xcd * (q + 1) : r * (q + 1) + (xcd - r) * q) + off; }
;         const int per = RT * CT, e = L / per, rem = L % per, pnl = rem / RT, pml = rem % RT;
;         u.pm = e * RT + pml; u.pn = e * CT + pnl; u.pc = pnl; u.hf = pml >= RTf ? 1 : 0; return true;
.LBB0_904:
	s_add_i32 s54, s54, 1
	v_readlane_b32 s4, v255, 9
	s_mul_i32 s0, s54, s50
	s_mul_hi_u32 s1, s54, s4
	s_add_i32 s1, s1, s0
	s_mul_i32 s0, s54, s4
	v_readlane_b32 s4, v255, 10
	s_add_u32 s24, s0, s4
	s_addc_u32 s25, s1, s45
	s_cmp_lg_u32 s54, 4
	s_cbranch_scc1 .Lp10_nobal
	v_readlane_b32 s65, v255, 9
	s_nop 0
	s_cmp_lg_u32 s65, 0x100
	s_cbranch_scc1 .Lp10_nobal
	s_lshr_b32 s64, s4, 3
	s_mov_b32 s65, 0x6633198f
	s_lshr_b32 s66, s65, s64
	s_and_b32 s66, s66, 1
	s_bfm_b32 s67, s64, 0
	s_and_b32 s67, s67, s65
	s_bcnt1_i32_b32 s67, s67
	s_add_i32 s64, s67, 0x7e
	s_cmp_gt_u32 s67, 7
	s_addc_u32 s64, s64, 0
	s_cmp_eq_u32 s67, 0
	s_cselect_b32 s64, 0x86, s64
	s_cmp_eq_u32 s67, 1
	s_cselect_b32 s64, 0x8f, s64
	s_lshl_b32 s64, s64, 3
	s_and_b32 s65, s4, 7
	s_or_b32 s64, s64, s65
	s_cmp_eq_u32 s66, 1
	s_cselect_b32 s24, s64, 0x480
	s_mov_b32 s25, 0
.Lp10_nobal:
	v_readlane_b32 s5, v255, 11
	v_mov_b64_e32 v[4:5], 0x480
	v_cmp_gt_i64_e64 s[0:1], s[24:25], v[240:241]
	v_cmp_lt_i64_e64 s[4:5], s[24:25], v[4:5]
	s_and_b64 vcc, exec, s[0:1]
	s_cbranch_vccnz .LBB0_906
	s_ashr_i32 s10, s24, 31
	s_lshr_b32 s10, s10, 29
	s_add_i32 s10, s24, s10
	s_ashr_i32 s18, s10, 3
	s_and_b32 s10, s10, -8
	s_sub_i32 s10, s24, s10
	s_cmp_lt_i32 s10, 0
	s_cselect_b32 s19, s46, 0x90
	s_mul_i32 s10, s10, s19
	s_add_i32 s10, s10, s18
	s_mul_hi_i32 s18, s10, 0x38e38e39
	s_lshr_b32 s19, s18, 31
	s_ashr_i32 s18, s18, 4
	s_add_i32 s19, s18, s19
	s_mul_i32 s18, s19, 0x48
	s_sub_i32 s10, s10, s18
	s_mul_i32 s18, s10, 57
	s_sext_i32_i16 s20, s18
	s_ashr_i32 s20, s20, 9
	s_bfe_u32 s18, s18, 0x1000f
	s_add_i32 s20, s20, s18
	s_sext_i32_i16 s18, s20
	s_mul_i32 s20, s20, 9
	s_sub_i32 s10, s10, s20
	s_bfe_i32 s21, s10, 0x80000
	s_sext_i32_i8 s10, s10
	s_mul_i32 s20, s19, 9
	s_add_i32 s20, s20, s10
	s_lshl_b32 s10, s19, 3
	s_add_i32 s55, s10, s18
	s_sext_i32_i16 s10, s21
	s_cmp_gt_i32 s10, 7
	s_cselect_b64 s[24:25], -1, 0
	v_cndmask_b32_e64 v3, 0, 1, s[24:25]
	s_nop 0
	v_readfirstlane_b32 s56, v3
